# gate/up GEMM: unit bias vector prefetched at unit start by one 16-lane LDS-DMA load into spare MISC LDS, epilogue reads it with ds_read_b128 (no global-load wait at epilogue start)
# baseline (speedup 1.0000x reference)
.LBB0_248:
	v_readlane_b32 s100, v254, 32
	v_and_b32_e32 v250, 3, v194
	v_lshlrev_b32_e32 v250, 5, v250
	v_bfe_u32 v251, v194, 2, 1
	v_lshl_or_b32 v250, v251, 4, v250
	v_bfe_u32 v251, v194, 3, 1
	v_lshl_or_b32 v250, v251, 12, v250
	s_and_b32 s101, s100, 3
	s_lshl_b32 s101, s101, 7
	v_add_u32_e32 v250, s101, v250
	s_lshl_b32 s101, s66, 9
	v_add_u32_e32 v250, s101, v250
	s_lshl_b32 s101, s68, 13
	v_add_u32_e32 v250, s101, v250
	v_mov_b32_e32 v231, s14
	v_add_co_u32_e32 v230, vcc, s5, v250
	s_nop 1
	v_addc_co_u32_e32 v231, vcc, 0, v231, vcc
	s_lshl_b32 s100, s100, 8
	s_add_i32 s100, s100, 0x23400
	v_lshrrev_b32_e32 v233, 4, v194
	v_lshl_add_u32 v233, v233, 4, s100
	s_mov_b32 m0, s100
	s_mov_b64 exec, 0xffff
	global_load_lds_dwordx4 v[230:231], off
	s_mov_b64 exec, -1
	s_ashr_i32 s63, s62, 31
	s_lshl_b64 s[36:37], s[62:63], 21
	s_add_u32 s4, s82, s36
	s_addc_u32 s6, s83, s37
	s_ashr_i32 s61, s60, 31
	s_lshl_b64 s[36:37], s[60:61], 18
	s_add_u32 s64, s4, s36
	s_addc_u32 s65, s6, s37
	s_and_b64 s[36:37], s[70:71], exec
	s_cselect_b32 s6, s65, s27
	s_cselect_b32 s31, s64, s26
	v_mov_b32_e32 v173, v1
	v_mov_b32_e32 v175, v1
	s_add_u32 s61, s26, 0x100
	v_lshl_add_u64 v[176:177], s[54:55], 0, v[174:175]
	v_lshl_add_u64 v[178:179], s[54:55], 0, v[172:173]
	s_addc_u32 s63, s27, 0
	s_mov_b32 s67, -2
	s_mov_b64 s[26:27], 0
	s_add_u32 s4, s46, s26
	s_addc_u32 s36, s47, s27
	s_add_u32 s69, s4, 0x2e000100
	s_addc_u32 s70, s36, 0
	s_add_u32 s74, s61, s26
	s_addc_u32 s86, s63, s27
	s_add_i32 s4, 0, 0x10000
	s_cmpk_eq_i32 s26, 0x300
	s_cselect_b64 vcc, -1, 0
	s_and_b64 s[36:37], vcc, exec
	s_cselect_b32 s71, s41, s70
	s_cselect_b32 s70, s40, s69
	v_add_u32_e32 v0, s4, v200
	s_cselect_b32 s37, s6, s86
	s_cselect_b32 s36, s31, s74
	s_add_i32 s69, 0, 0x14000
	ds_read_b128 v[18:21], v0
	ds_read_b128 v[22:25], v0 offset:1024
	ds_read_b128 v[26:29], v0 offset:2048
	ds_read_b128 v[30:33], v0 offset:3072
	v_add_u32_e32 v0, s69, v200
	ds_read_b128 v[2:5], v0
	ds_read_b128 v[6:9], v0 offset:1024
	ds_read_b128 v[10:13], v0 offset:2048
	ds_read_b128 v[14:17], v0 offset:3072
	v_lshl_add_u64 v[222:223], v[178:179], 0, s[26:27]
	s_add_i32 m0, s93, 0xc000
	ds_read_b128 v[180:183], v201
	ds_read_b128 v[184:187], v201 offset:1024
	ds_read_b128 v[206:209], v201 offset:2048
	ds_read_b128 v[210:213], v201 offset:3072
	ds_read_b128 v[214:217], v201 offset:4096
	ds_read_b128 v[218:221], v201 offset:5120
	ds_read_b128 v[234:237], v201 offset:6144
	ds_read_b128 v[238:241], v201 offset:7168
	global_load_lds_dwordx4 v[222:223], off
	v_lshl_add_u64 v[222:223], v[176:177], 0, s[26:27]
	s_add_i32 m0, s93, 0xe000
	s_nop 0
	global_load_lds_dwordx4 v[222:223], off
	s_waitcnt vmcnt(8)
	s_waitcnt lgkmcnt(0)
	s_barrier
	s_setprio 1
	s_waitcnt lgkmcnt(0)
	v_mfma_scale_f32_16x16x128_f8f6f4 v[158:161], v[18:25], v[180:187], 0, v191, v191 op_sel_hi:[0,0,0]
	v_mfma_scale_f32_16x16x128_f8f6f4 v[154:157], v[26:33], v[180:187], 0, v191, v191 op_sel_hi:[0,0,0]
	v_mfma_scale_f32_16x16x128_f8f6f4 v[142:145], v[18:25], v[206:213], 0, v191, v191 op_sel_hi:[0,0,0]
	v_mfma_scale_f32_16x16x128_f8f6f4 v[138:141], v[26:33], v[206:213], 0, v191, v191 op_sel_hi:[0,0,0]
	v_mfma_scale_f32_16x16x128_f8f6f4 v[126:129], v[18:25], v[214:221], 0, v191, v191 op_sel_hi:[0,0,0]
	v_mfma_scale_f32_16x16x128_f8f6f4 v[122:125], v[26:33], v[214:221], 0, v191, v191 op_sel_hi:[0,0,0]
	v_mfma_scale_f32_16x16x128_f8f6f4 v[110:113], v[18:25], v[234:241], 0, v191, v191 op_sel_hi:[0,0,0]
	v_mfma_scale_f32_16x16x128_f8f6f4 v[106:109], v[26:33], v[234:241], 0, v191, v191 op_sel_hi:[0,0,0]
	s_setprio 0
	s_setprio 1
	v_mfma_scale_f32_16x16x128_f8f6f4 v[150:153], v[2:9], v[180:187], 0, v191, v191 op_sel_hi:[0,0,0]
	v_mfma_scale_f32_16x16x128_f8f6f4 v[146:149], v[10:17], v[180:187], 0, v191, v191 op_sel_hi:[0,0,0]
	v_mfma_scale_f32_16x16x128_f8f6f4 v[134:137], v[2:9], v[206:213], 0, v191, v191 op_sel_hi:[0,0,0]
	v_mfma_scale_f32_16x16x128_f8f6f4 v[130:133], v[10:17], v[206:213], 0, v191, v191 op_sel_hi:[0,0,0]
	v_mfma_scale_f32_16x16x128_f8f6f4 v[118:121], v[2:9], v[214:221], 0, v191, v191 op_sel_hi:[0,0,0]
	v_mfma_scale_f32_16x16x128_f8f6f4 v[114:117], v[10:17], v[214:221], 0, v191, v191 op_sel_hi:[0,0,0]
	v_mfma_scale_f32_16x16x128_f8f6f4 v[102:105], v[2:9], v[234:241], 0, v191, v191 op_sel_hi:[0,0,0]
	v_mfma_scale_f32_16x16x128_f8f6f4 v[98:101], v[10:17], v[234:241], 0, v191, v191 op_sel_hi:[0,0,0]
	s_setprio 0
	s_barrier
	s_add_i32 s4, s4, s92
	v_lshl_add_u64 v[180:181], s[36:37], 0, v[162:163]
	s_mov_b32 m0, s4
	ds_read_b128 v[206:209], v201 offset:16384
	ds_read_b128 v[210:213], v201 offset:17408
	ds_read_b128 v[214:217], v201 offset:18432
	ds_read_b128 v[218:221], v201 offset:19456
	ds_read_b128 v[234:237], v201 offset:20480
	ds_read_b128 v[238:241], v201 offset:21504
	ds_read_b128 v[242:245], v201 offset:22528
	ds_read_b128 v[246:249], v201 offset:23552
	global_load_lds_dwordx4 v[180:181], off
	s_add_i32 m0, s4, 0x2000
	s_add_u32 s86, s36, 0x20000
	v_lshl_add_u64 v[182:183], s[36:37], 0, v[164:165]
	s_addc_u32 s87, s37, 0
	s_add_i32 s4, s69, s92
	global_load_lds_dwordx4 v[182:183], off
	v_lshl_add_u64 v[184:185], s[86:87], 0, v[162:163]
	s_mov_b32 m0, s4
	v_cndmask_b32_e32 v0, v168, v202, vcc
	global_load_lds_dwordx4 v[184:185], off
	v_lshl_add_u64 v[184:185], s[86:87], 0, v[164:165]
	s_add_i32 m0, s4, 0x2000
	v_lshl_add_u64 v[186:187], s[70:71], 0, v[0:1]
	global_load_lds_dwordx4 v[184:185], off
	s_mov_b32 m0, s93
	v_cndmask_b32_e32 v184, v170, v203, vcc
	global_load_lds_dwordx4 v0, s[70:71]
	s_mov_b32 m0, s79
	v_mov_b32_e32 v185, v1
	global_load_lds_dwordx4 v184, s[70:71]
	s_waitcnt vmcnt(8)
	s_waitcnt lgkmcnt(0)
	v_lshl_add_u64 v[184:185], s[70:71], 0, v[184:185]
	s_barrier
	s_setprio 1
	s_waitcnt lgkmcnt(0)
	v_mfma_scale_f32_16x16x128_f8f6f4 v[94:97], v[18:25], v[206:213], 0, v191, v191 op_sel_hi:[0,0,0]
	v_mfma_scale_f32_16x16x128_f8f6f4 v[90:93], v[26:33], v[206:213], 0, v191, v191 op_sel_hi:[0,0,0]
	v_mfma_scale_f32_16x16x128_f8f6f4 v[70:73], v[18:25], v[214:221], 0, v191, v191 op_sel_hi:[0,0,0]
	v_mfma_scale_f32_16x16x128_f8f6f4 v[66:69], v[26:33], v[214:221], 0, v191, v191 op_sel_hi:[0,0,0]
	v_mfma_scale_f32_16x16x128_f8f6f4 v[54:57], v[18:25], v[234:241], 0, v191, v191 op_sel_hi:[0,0,0]
	v_mfma_scale_f32_16x16x128_f8f6f4 v[50:53], v[26:33], v[234:241], 0, v191, v191 op_sel_hi:[0,0,0]
	v_mfma_scale_f32_16x16x128_f8f6f4 v[38:41], v[18:25], v[242:249], 0, v191, v191 op_sel_hi:[0,0,0]
	v_mfma_scale_f32_16x16x128_f8f6f4 v[34:37], v[26:33], v[242:249], 0, v191, v191 op_sel_hi:[0,0,0]
	s_setprio 0
	s_setprio 1
	v_mfma_scale_f32_16x16x128_f8f6f4 v[86:89], v[2:9], v[206:213], 0, v191, v191 op_sel_hi:[0,0,0]
	v_mfma_scale_f32_16x16x128_f8f6f4 v[82:85], v[10:17], v[206:213], 0, v191, v191 op_sel_hi:[0,0,0]
	v_mfma_scale_f32_16x16x128_f8f6f4 v[78:81], v[2:9], v[214:221], 0, v191, v191 op_sel_hi:[0,0,0]
	v_mfma_scale_f32_16x16x128_f8f6f4 v[74:77], v[10:17], v[214:221], 0, v191, v191 op_sel_hi:[0,0,0]
	v_mfma_scale_f32_16x16x128_f8f6f4 v[62:65], v[2:9], v[234:241], 0, v191, v191 op_sel_hi:[0,0,0]
	v_mfma_scale_f32_16x16x128_f8f6f4 v[58:61], v[10:17], v[234:241], 0, v191, v191 op_sel_hi:[0,0,0]
	v_mfma_scale_f32_16x16x128_f8f6f4 v[46:49], v[2:9], v[242:249], 0, v191, v191 op_sel_hi:[0,0,0]
	v_mfma_scale_f32_16x16x128_f8f6f4 v[42:45], v[10:17], v[242:249], 0, v191, v191 op_sel_hi:[0,0,0]
	s_setprio 0
	s_barrier
	s_add_i32 s4, 0, 0x18000
	v_add_u32_e32 v0, s4, v200
	s_add_i32 s69, 0, 0x1c000
	ds_read_b128 v[2:5], v0
	ds_read_b128 v[6:9], v0 offset:1024
	ds_read_b128 v[10:13], v0 offset:2048
	ds_read_b128 v[14:17], v0 offset:3072
	v_add_u32_e32 v0, s69, v200
	ds_read_b128 v[18:21], v0
	ds_read_b128 v[22:25], v0 offset:1024
	ds_read_b128 v[26:29], v0 offset:2048
	ds_read_b128 v[30:33], v0 offset:3072
	s_mov_b32 m0, s84
	v_cndmask_b32_e32 v0, v172, v204, vcc
	ds_read_b128 v[206:209], v201 offset:32768
	ds_read_b128 v[210:213], v201 offset:33792
	ds_read_b128 v[214:217], v201 offset:34816
	ds_read_b128 v[218:221], v201 offset:35840
	ds_read_b128 v[234:237], v201 offset:36864
	ds_read_b128 v[238:241], v201 offset:37888
	ds_read_b128 v[242:245], v201 offset:38912
	ds_read_b128 v[246:249], v201 offset:39936
	v_cndmask_b32_e32 v173, v174, v205, vcc
	global_load_lds_dwordx4 v0, s[70:71]
	s_mov_b32 m0, s85
	s_nop 0
	global_load_lds_dwordx4 v173, s[70:71]
	s_waitcnt vmcnt(8)
	s_waitcnt lgkmcnt(0)
	s_barrier
	s_setprio 1
	s_waitcnt lgkmcnt(0)
	v_mfma_scale_f32_16x16x128_f8f6f4 v[158:161], v[2:9], v[206:213], v[158:161], v191, v191 op_sel_hi:[0,0,0]
	v_mfma_scale_f32_16x16x128_f8f6f4 v[154:157], v[10:17], v[206:213], v[154:157], v191, v191 op_sel_hi:[0,0,0]
	v_mfma_scale_f32_16x16x128_f8f6f4 v[142:145], v[2:9], v[214:221], v[142:145], v191, v191 op_sel_hi:[0,0,0]
	v_mfma_scale_f32_16x16x128_f8f6f4 v[138:141], v[10:17], v[214:221], v[138:141], v191, v191 op_sel_hi:[0,0,0]
	v_mfma_scale_f32_16x16x128_f8f6f4 v[126:129], v[2:9], v[234:241], v[126:129], v191, v191 op_sel_hi:[0,0,0]
	v_mfma_scale_f32_16x16x128_f8f6f4 v[122:125], v[10:17], v[234:241], v[122:125], v191, v191 op_sel_hi:[0,0,0]
	v_mfma_scale_f32_16x16x128_f8f6f4 v[110:113], v[2:9], v[242:249], v[110:113], v191, v191 op_sel_hi:[0,0,0]
	v_mfma_scale_f32_16x16x128_f8f6f4 v[106:109], v[10:17], v[242:249], v[106:109], v191, v191 op_sel_hi:[0,0,0]
	s_setprio 0
	s_setprio 1
	v_mfma_scale_f32_16x16x128_f8f6f4 v[150:153], v[18:25], v[206:213], v[150:153], v191, v191 op_sel_hi:[0,0,0]
	v_mfma_scale_f32_16x16x128_f8f6f4 v[146:149], v[26:33], v[206:213], v[146:149], v191, v191 op_sel_hi:[0,0,0]
	v_mfma_scale_f32_16x16x128_f8f6f4 v[134:137], v[18:25], v[214:221], v[134:137], v191, v191 op_sel_hi:[0,0,0]
	v_mfma_scale_f32_16x16x128_f8f6f4 v[130:133], v[26:33], v[214:221], v[130:133], v191, v191 op_sel_hi:[0,0,0]
	v_mfma_scale_f32_16x16x128_f8f6f4 v[118:121], v[18:25], v[234:241], v[118:121], v191, v191 op_sel_hi:[0,0,0]
	v_mfma_scale_f32_16x16x128_f8f6f4 v[114:117], v[26:33], v[234:241], v[114:117], v191, v191 op_sel_hi:[0,0,0]
	v_mfma_scale_f32_16x16x128_f8f6f4 v[102:105], v[18:25], v[242:249], v[102:105], v191, v191 op_sel_hi:[0,0,0]
	v_mfma_scale_f32_16x16x128_f8f6f4 v[98:101], v[26:33], v[242:249], v[98:101], v191, v191 op_sel_hi:[0,0,0]
	s_setprio 0
	s_barrier
	s_add_i32 s4, s4, s92
	v_lshl_add_u64 v[180:181], v[180:181], 0, s[22:23]
	s_mov_b32 m0, s4
	ds_read_b128 v[206:209], v201 offset:49152
	ds_read_b128 v[210:213], v201 offset:50176
	ds_read_b128 v[214:217], v201 offset:51200
	ds_read_b128 v[218:221], v201 offset:52224
	ds_read_b128 v[234:237], v201 offset:53248
	ds_read_b128 v[238:241], v201 offset:54272
	ds_read_b128 v[242:245], v201 offset:55296
	ds_read_b128 v[246:249], v201 offset:56320
	global_load_lds_dwordx4 v[180:181], off
	s_add_i32 m0, s4, 0x2000
	s_add_u32 s36, s36, 0x20080
	v_lshl_add_u64 v[180:181], v[182:183], 0, s[22:23]
	s_addc_u32 s37, s37, 0
	s_add_i32 s4, s69, s92
	global_load_lds_dwordx4 v[180:181], off
	v_lshl_add_u64 v[180:181], s[36:37], 0, v[162:163]
	s_mov_b32 m0, s4
	s_nop 0
	global_load_lds_dwordx4 v[180:181], off
	v_lshl_add_u64 v[180:181], s[36:37], 0, v[164:165]
	s_add_i32 m0, s4, 0x2000
	s_nop 0
	global_load_lds_dwordx4 v[180:181], off
	v_lshl_add_u64 v[180:181], v[186:187], 0, s[22:23]
	s_mov_b32 m0, s15
	s_nop 0
	global_load_lds_dwordx4 v[180:181], off
	v_lshl_add_u64 v[180:181], v[184:185], 0, s[22:23]
	s_mov_b32 m0, s16
	s_nop 0
	global_load_lds_dwordx4 v[180:181], off
	s_waitcnt vmcnt(8)
	s_waitcnt lgkmcnt(0)
	s_barrier
	s_setprio 1
	s_waitcnt lgkmcnt(0)
	v_mfma_scale_f32_16x16x128_f8f6f4 v[94:97], v[2:9], v[206:213], v[94:97], v191, v191 op_sel_hi:[0,0,0]
	v_mfma_scale_f32_16x16x128_f8f6f4 v[90:93], v[10:17], v[206:213], v[90:93], v191, v191 op_sel_hi:[0,0,0]
	v_mfma_scale_f32_16x16x128_f8f6f4 v[70:73], v[2:9], v[214:221], v[70:73], v191, v191 op_sel_hi:[0,0,0]
	v_mfma_scale_f32_16x16x128_f8f6f4 v[66:69], v[10:17], v[214:221], v[66:69], v191, v191 op_sel_hi:[0,0,0]
	v_mfma_scale_f32_16x16x128_f8f6f4 v[54:57], v[2:9], v[234:241], v[54:57], v191, v191 op_sel_hi:[0,0,0]
	v_mfma_scale_f32_16x16x128_f8f6f4 v[50:53], v[10:17], v[234:241], v[50:53], v191, v191 op_sel_hi:[0,0,0]
	v_mfma_scale_f32_16x16x128_f8f6f4 v[38:41], v[2:9], v[242:249], v[38:41], v191, v191 op_sel_hi:[0,0,0]
	v_mfma_scale_f32_16x16x128_f8f6f4 v[34:37], v[10:17], v[242:249], v[34:37], v191, v191 op_sel_hi:[0,0,0]
	s_setprio 0
	s_setprio 1
	v_mfma_scale_f32_16x16x128_f8f6f4 v[86:89], v[18:25], v[206:213], v[86:89], v191, v191 op_sel_hi:[0,0,0]
	v_mfma_scale_f32_16x16x128_f8f6f4 v[82:85], v[26:33], v[206:213], v[82:85], v191, v191 op_sel_hi:[0,0,0]
	v_mfma_scale_f32_16x16x128_f8f6f4 v[78:81], v[18:25], v[214:221], v[78:81], v191, v191 op_sel_hi:[0,0,0]
	v_mfma_scale_f32_16x16x128_f8f6f4 v[74:77], v[26:33], v[214:221], v[74:77], v191, v191 op_sel_hi:[0,0,0]
	v_mfma_scale_f32_16x16x128_f8f6f4 v[62:65], v[18:25], v[234:241], v[62:65], v191, v191 op_sel_hi:[0,0,0]
	v_mfma_scale_f32_16x16x128_f8f6f4 v[58:61], v[26:33], v[234:241], v[58:61], v191, v191 op_sel_hi:[0,0,0]
	v_mfma_scale_f32_16x16x128_f8f6f4 v[46:49], v[18:25], v[242:249], v[46:49], v191, v191 op_sel_hi:[0,0,0]
	v_mfma_scale_f32_16x16x128_f8f6f4 v[42:45], v[26:33], v[242:249], v[42:45], v191, v191 op_sel_hi:[0,0,0]
	s_setprio 0
	s_barrier
	s_add_i32 s67, s67, 2
	s_add_u32 s26, s26, 0x100
	s_addc_u32 s27, s27, 0
.LBB0_249:
	s_add_u32 s4, s46, s26
	s_addc_u32 s36, s47, s27
	s_add_u32 s69, s4, 0x2e000100
	s_addc_u32 s70, s36, 0
	s_add_u32 s74, s61, s26
	s_addc_u32 s86, s63, s27
	s_add_i32 s4, 0, 0x10000
	s_cmpk_eq_i32 s26, 0x300
	s_cselect_b64 vcc, -1, 0
	s_and_b64 s[36:37], vcc, exec
	s_cselect_b32 s71, s41, s70
	s_cselect_b32 s70, s40, s69
	v_add_u32_e32 v0, s4, v200
	s_cselect_b32 s37, s6, s86
	s_cselect_b32 s36, s31, s74
	s_add_i32 s69, 0, 0x14000
	ds_read_b128 v[18:21], v0
	ds_read_b128 v[22:25], v0 offset:1024
	ds_read_b128 v[26:29], v0 offset:2048
	ds_read_b128 v[30:33], v0 offset:3072
	v_add_u32_e32 v0, s69, v200
	ds_read_b128 v[2:5], v0
	ds_read_b128 v[6:9], v0 offset:1024
	ds_read_b128 v[10:13], v0 offset:2048
	ds_read_b128 v[14:17], v0 offset:3072
	v_lshl_add_u64 v[222:223], v[178:179], 0, s[26:27]
	s_add_i32 m0, s93, 0xc000
	ds_read_b128 v[180:183], v201
	ds_read_b128 v[184:187], v201 offset:1024
	ds_read_b128 v[206:209], v201 offset:2048
	ds_read_b128 v[210:213], v201 offset:3072
	ds_read_b128 v[214:217], v201 offset:4096
	ds_read_b128 v[218:221], v201 offset:5120
	ds_read_b128 v[234:237], v201 offset:6144
	ds_read_b128 v[238:241], v201 offset:7168
	global_load_lds_dwordx4 v[222:223], off
	v_lshl_add_u64 v[222:223], v[176:177], 0, s[26:27]
	s_add_i32 m0, s93, 0xe000
	s_nop 0
	global_load_lds_dwordx4 v[222:223], off
	s_waitcnt vmcnt(8)
	s_waitcnt lgkmcnt(0)
	s_barrier
	s_setprio 1
	s_waitcnt lgkmcnt(0)
	v_mfma_scale_f32_16x16x128_f8f6f4 v[158:161], v[18:25], v[180:187], v[158:161], v191, v191 op_sel_hi:[0,0,0]
	v_mfma_scale_f32_16x16x128_f8f6f4 v[154:157], v[26:33], v[180:187], v[154:157], v191, v191 op_sel_hi:[0,0,0]
	v_mfma_scale_f32_16x16x128_f8f6f4 v[142:145], v[18:25], v[206:213], v[142:145], v191, v191 op_sel_hi:[0,0,0]
	v_mfma_scale_f32_16x16x128_f8f6f4 v[138:141], v[26:33], v[206:213], v[138:141], v191, v191 op_sel_hi:[0,0,0]
	v_mfma_scale_f32_16x16x128_f8f6f4 v[126:129], v[18:25], v[214:221], v[126:129], v191, v191 op_sel_hi:[0,0,0]
	v_mfma_scale_f32_16x16x128_f8f6f4 v[122:125], v[26:33], v[214:221], v[122:125], v191, v191 op_sel_hi:[0,0,0]
	v_mfma_scale_f32_16x16x128_f8f6f4 v[110:113], v[18:25], v[234:241], v[110:113], v191, v191 op_sel_hi:[0,0,0]
	v_mfma_scale_f32_16x16x128_f8f6f4 v[106:109], v[26:33], v[234:241], v[106:109], v191, v191 op_sel_hi:[0,0,0]
	s_setprio 0
	s_setprio 1
	v_mfma_scale_f32_16x16x128_f8f6f4 v[150:153], v[2:9], v[180:187], v[150:153], v191, v191 op_sel_hi:[0,0,0]
	v_mfma_scale_f32_16x16x128_f8f6f4 v[146:149], v[10:17], v[180:187], v[146:149], v191, v191 op_sel_hi:[0,0,0]
	v_mfma_scale_f32_16x16x128_f8f6f4 v[134:137], v[2:9], v[206:213], v[134:137], v191, v191 op_sel_hi:[0,0,0]
	v_mfma_scale_f32_16x16x128_f8f6f4 v[130:133], v[10:17], v[206:213], v[130:133], v191, v191 op_sel_hi:[0,0,0]
	v_mfma_scale_f32_16x16x128_f8f6f4 v[118:121], v[2:9], v[214:221], v[118:121], v191, v191 op_sel_hi:[0,0,0]
	v_mfma_scale_f32_16x16x128_f8f6f4 v[114:117], v[10:17], v[214:221], v[114:117], v191, v191 op_sel_hi:[0,0,0]
	v_mfma_scale_f32_16x16x128_f8f6f4 v[102:105], v[2:9], v[234:241], v[102:105], v191, v191 op_sel_hi:[0,0,0]
	v_mfma_scale_f32_16x16x128_f8f6f4 v[98:101], v[10:17], v[234:241], v[98:101], v191, v191 op_sel_hi:[0,0,0]
	s_setprio 0
	s_barrier
	s_add_i32 s4, s4, s92
	v_lshl_add_u64 v[180:181], s[36:37], 0, v[162:163]
	s_mov_b32 m0, s4
	ds_read_b128 v[206:209], v201 offset:16384
	ds_read_b128 v[210:213], v201 offset:17408
	ds_read_b128 v[214:217], v201 offset:18432
	ds_read_b128 v[218:221], v201 offset:19456
	ds_read_b128 v[234:237], v201 offset:20480
	ds_read_b128 v[238:241], v201 offset:21504
	ds_read_b128 v[242:245], v201 offset:22528
	ds_read_b128 v[246:249], v201 offset:23552
	global_load_lds_dwordx4 v[180:181], off
	s_add_i32 m0, s4, 0x2000
	s_add_u32 s86, s36, 0x20000
	v_lshl_add_u64 v[182:183], s[36:37], 0, v[164:165]
	s_addc_u32 s87, s37, 0
	s_add_i32 s4, s69, s92
	global_load_lds_dwordx4 v[182:183], off
	v_lshl_add_u64 v[184:185], s[86:87], 0, v[162:163]
	s_mov_b32 m0, s4
	v_cndmask_b32_e32 v0, v168, v202, vcc
	global_load_lds_dwordx4 v[184:185], off
	v_lshl_add_u64 v[184:185], s[86:87], 0, v[164:165]
	s_add_i32 m0, s4, 0x2000
	v_lshl_add_u64 v[186:187], s[70:71], 0, v[0:1]
	global_load_lds_dwordx4 v[184:185], off
	s_mov_b32 m0, s93
	v_cndmask_b32_e32 v184, v170, v203, vcc
	global_load_lds_dwordx4 v0, s[70:71]
	s_mov_b32 m0, s79
	v_mov_b32_e32 v185, v1
	global_load_lds_dwordx4 v184, s[70:71]
	s_waitcnt vmcnt(8)
	s_waitcnt lgkmcnt(0)
	v_lshl_add_u64 v[184:185], s[70:71], 0, v[184:185]
	s_barrier
	s_setprio 1
	s_waitcnt lgkmcnt(0)
	v_mfma_scale_f32_16x16x128_f8f6f4 v[94:97], v[18:25], v[206:213], v[94:97], v191, v191 op_sel_hi:[0,0,0]
	v_mfma_scale_f32_16x16x128_f8f6f4 v[90:93], v[26:33], v[206:213], v[90:93], v191, v191 op_sel_hi:[0,0,0]
	v_mfma_scale_f32_16x16x128_f8f6f4 v[70:73], v[18:25], v[214:221], v[70:73], v191, v191 op_sel_hi:[0,0,0]
	v_mfma_scale_f32_16x16x128_f8f6f4 v[66:69], v[26:33], v[214:221], v[66:69], v191, v191 op_sel_hi:[0,0,0]
	v_mfma_scale_f32_16x16x128_f8f6f4 v[54:57], v[18:25], v[234:241], v[54:57], v191, v191 op_sel_hi:[0,0,0]
	v_mfma_scale_f32_16x16x128_f8f6f4 v[50:53], v[26:33], v[234:241], v[50:53], v191, v191 op_sel_hi:[0,0,0]
	v_mfma_scale_f32_16x16x128_f8f6f4 v[38:41], v[18:25], v[242:249], v[38:41], v191, v191 op_sel_hi:[0,0,0]
	v_mfma_scale_f32_16x16x128_f8f6f4 v[34:37], v[26:33], v[242:249], v[34:37], v191, v191 op_sel_hi:[0,0,0]
	s_setprio 0
	s_setprio 1
	v_mfma_scale_f32_16x16x128_f8f6f4 v[86:89], v[2:9], v[206:213], v[86:89], v191, v191 op_sel_hi:[0,0,0]
	v_mfma_scale_f32_16x16x128_f8f6f4 v[82:85], v[10:17], v[206:213], v[82:85], v191, v191 op_sel_hi:[0,0,0]
	v_mfma_scale_f32_16x16x128_f8f6f4 v[78:81], v[2:9], v[214:221], v[78:81], v191, v191 op_sel_hi:[0,0,0]
	v_mfma_scale_f32_16x16x128_f8f6f4 v[74:77], v[10:17], v[214:221], v[74:77], v191, v191 op_sel_hi:[0,0,0]
	v_mfma_scale_f32_16x16x128_f8f6f4 v[62:65], v[2:9], v[234:241], v[62:65], v191, v191 op_sel_hi:[0,0,0]
	v_mfma_scale_f32_16x16x128_f8f6f4 v[58:61], v[10:17], v[234:241], v[58:61], v191, v191 op_sel_hi:[0,0,0]
	v_mfma_scale_f32_16x16x128_f8f6f4 v[46:49], v[2:9], v[242:249], v[46:49], v191, v191 op_sel_hi:[0,0,0]
	v_mfma_scale_f32_16x16x128_f8f6f4 v[42:45], v[10:17], v[242:249], v[42:45], v191, v191 op_sel_hi:[0,0,0]
	s_setprio 0
	s_barrier
	s_add_i32 s4, 0, 0x18000
	v_add_u32_e32 v0, s4, v200
	s_add_i32 s69, 0, 0x1c000
	ds_read_b128 v[2:5], v0
	ds_read_b128 v[6:9], v0 offset:1024
	ds_read_b128 v[10:13], v0 offset:2048
	ds_read_b128 v[14:17], v0 offset:3072
	v_add_u32_e32 v0, s69, v200
	ds_read_b128 v[18:21], v0
	ds_read_b128 v[22:25], v0 offset:1024
	ds_read_b128 v[26:29], v0 offset:2048
	ds_read_b128 v[30:33], v0 offset:3072
	s_mov_b32 m0, s84
	v_cndmask_b32_e32 v0, v172, v204, vcc
	ds_read_b128 v[206:209], v201 offset:32768
	ds_read_b128 v[210:213], v201 offset:33792
	ds_read_b128 v[214:217], v201 offset:34816
	ds_read_b128 v[218:221], v201 offset:35840
	ds_read_b128 v[234:237], v201 offset:36864
	ds_read_b128 v[238:241], v201 offset:37888
	ds_read_b128 v[242:245], v201 offset:38912
	ds_read_b128 v[246:249], v201 offset:39936
	v_cndmask_b32_e32 v173, v174, v205, vcc
	global_load_lds_dwordx4 v0, s[70:71]
	s_mov_b32 m0, s85
	s_nop 0
	global_load_lds_dwordx4 v173, s[70:71]
	s_waitcnt vmcnt(8)
	s_waitcnt lgkmcnt(0)
	s_barrier
	s_setprio 1
	s_waitcnt lgkmcnt(0)
	v_mfma_scale_f32_16x16x128_f8f6f4 v[158:161], v[2:9], v[206:213], v[158:161], v191, v191 op_sel_hi:[0,0,0]
	v_mfma_scale_f32_16x16x128_f8f6f4 v[154:157], v[10:17], v[206:213], v[154:157], v191, v191 op_sel_hi:[0,0,0]
	v_mfma_scale_f32_16x16x128_f8f6f4 v[142:145], v[2:9], v[214:221], v[142:145], v191, v191 op_sel_hi:[0,0,0]
	v_mfma_scale_f32_16x16x128_f8f6f4 v[138:141], v[10:17], v[214:221], v[138:141], v191, v191 op_sel_hi:[0,0,0]
	v_mfma_scale_f32_16x16x128_f8f6f4 v[126:129], v[2:9], v[234:241], v[126:129], v191, v191 op_sel_hi:[0,0,0]
	v_mfma_scale_f32_16x16x128_f8f6f4 v[122:125], v[10:17], v[234:241], v[122:125], v191, v191 op_sel_hi:[0,0,0]
	v_mfma_scale_f32_16x16x128_f8f6f4 v[110:113], v[2:9], v[242:249], v[110:113], v191, v191 op_sel_hi:[0,0,0]
	v_mfma_scale_f32_16x16x128_f8f6f4 v[106:109], v[10:17], v[242:249], v[106:109], v191, v191 op_sel_hi:[0,0,0]
	s_setprio 0
	s_setprio 1
	v_mfma_scale_f32_16x16x128_f8f6f4 v[150:153], v[18:25], v[206:213], v[150:153], v191, v191 op_sel_hi:[0,0,0]
	v_mfma_scale_f32_16x16x128_f8f6f4 v[146:149], v[26:33], v[206:213], v[146:149], v191, v191 op_sel_hi:[0,0,0]
	v_mfma_scale_f32_16x16x128_f8f6f4 v[134:137], v[18:25], v[214:221], v[134:137], v191, v191 op_sel_hi:[0,0,0]
	v_mfma_scale_f32_16x16x128_f8f6f4 v[130:133], v[26:33], v[214:221], v[130:133], v191, v191 op_sel_hi:[0,0,0]
	v_mfma_scale_f32_16x16x128_f8f6f4 v[118:121], v[18:25], v[234:241], v[118:121], v191, v191 op_sel_hi:[0,0,0]
	v_mfma_scale_f32_16x16x128_f8f6f4 v[114:117], v[26:33], v[234:241], v[114:117], v191, v191 op_sel_hi:[0,0,0]
	v_mfma_scale_f32_16x16x128_f8f6f4 v[102:105], v[18:25], v[242:249], v[102:105], v191, v191 op_sel_hi:[0,0,0]
	v_mfma_scale_f32_16x16x128_f8f6f4 v[98:101], v[26:33], v[242:249], v[98:101], v191, v191 op_sel_hi:[0,0,0]
	s_setprio 0
	s_barrier
	s_add_i32 s4, s4, s92
	v_lshl_add_u64 v[180:181], v[180:181], 0, s[22:23]
	s_mov_b32 m0, s4
	ds_read_b128 v[206:209], v201 offset:49152
	ds_read_b128 v[210:213], v201 offset:50176
	ds_read_b128 v[214:217], v201 offset:51200
	ds_read_b128 v[218:221], v201 offset:52224
	ds_read_b128 v[234:237], v201 offset:53248
	ds_read_b128 v[238:241], v201 offset:54272
	ds_read_b128 v[242:245], v201 offset:55296
	ds_read_b128 v[246:249], v201 offset:56320
	global_load_lds_dwordx4 v[180:181], off
	s_add_i32 m0, s4, 0x2000
	s_add_u32 s36, s36, 0x20080
	v_lshl_add_u64 v[180:181], v[182:183], 0, s[22:23]
	s_addc_u32 s37, s37, 0
	s_add_i32 s4, s69, s92
	global_load_lds_dwordx4 v[180:181], off
	v_lshl_add_u64 v[180:181], s[36:37], 0, v[162:163]
	s_mov_b32 m0, s4
	s_nop 0
	global_load_lds_dwordx4 v[180:181], off
	v_lshl_add_u64 v[180:181], s[36:37], 0, v[164:165]
	s_add_i32 m0, s4, 0x2000
	s_nop 0
	global_load_lds_dwordx4 v[180:181], off
	v_lshl_add_u64 v[180:181], v[186:187], 0, s[22:23]
	s_mov_b32 m0, s15
	s_nop 0
	global_load_lds_dwordx4 v[180:181], off
	v_lshl_add_u64 v[180:181], v[184:185], 0, s[22:23]
	s_mov_b32 m0, s16
	s_nop 0
	global_load_lds_dwordx4 v[180:181], off
	s_waitcnt vmcnt(8)
	s_waitcnt lgkmcnt(0)
	s_barrier
	s_setprio 1
	s_waitcnt lgkmcnt(0)
	v_mfma_scale_f32_16x16x128_f8f6f4 v[94:97], v[2:9], v[206:213], v[94:97], v191, v191 op_sel_hi:[0,0,0]
	v_mfma_scale_f32_16x16x128_f8f6f4 v[90:93], v[10:17], v[206:213], v[90:93], v191, v191 op_sel_hi:[0,0,0]
	v_mfma_scale_f32_16x16x128_f8f6f4 v[70:73], v[2:9], v[214:221], v[70:73], v191, v191 op_sel_hi:[0,0,0]
	v_mfma_scale_f32_16x16x128_f8f6f4 v[66:69], v[10:17], v[214:221], v[66:69], v191, v191 op_sel_hi:[0,0,0]
	v_mfma_scale_f32_16x16x128_f8f6f4 v[54:57], v[2:9], v[234:241], v[54:57], v191, v191 op_sel_hi:[0,0,0]
	v_mfma_scale_f32_16x16x128_f8f6f4 v[50:53], v[10:17], v[234:241], v[50:53], v191, v191 op_sel_hi:[0,0,0]
	v_mfma_scale_f32_16x16x128_f8f6f4 v[38:41], v[2:9], v[242:249], v[38:41], v191, v191 op_sel_hi:[0,0,0]
	v_mfma_scale_f32_16x16x128_f8f6f4 v[34:37], v[10:17], v[242:249], v[34:37], v191, v191 op_sel_hi:[0,0,0]
	s_setprio 0
	s_setprio 1
	v_mfma_scale_f32_16x16x128_f8f6f4 v[86:89], v[18:25], v[206:213], v[86:89], v191, v191 op_sel_hi:[0,0,0]
	v_mfma_scale_f32_16x16x128_f8f6f4 v[82:85], v[26:33], v[206:213], v[82:85], v191, v191 op_sel_hi:[0,0,0]
	v_mfma_scale_f32_16x16x128_f8f6f4 v[78:81], v[18:25], v[214:221], v[78:81], v191, v191 op_sel_hi:[0,0,0]
	v_mfma_scale_f32_16x16x128_f8f6f4 v[74:77], v[26:33], v[214:221], v[74:77], v191, v191 op_sel_hi:[0,0,0]
	v_mfma_scale_f32_16x16x128_f8f6f4 v[62:65], v[18:25], v[234:241], v[62:65], v191, v191 op_sel_hi:[0,0,0]
	v_mfma_scale_f32_16x16x128_f8f6f4 v[58:61], v[26:33], v[234:241], v[58:61], v191, v191 op_sel_hi:[0,0,0]
	v_mfma_scale_f32_16x16x128_f8f6f4 v[46:49], v[18:25], v[242:249], v[46:49], v191, v191 op_sel_hi:[0,0,0]
	v_mfma_scale_f32_16x16x128_f8f6f4 v[42:45], v[26:33], v[242:249], v[42:45], v191, v191 op_sel_hi:[0,0,0]
	s_setprio 0
	s_barrier
	s_add_i32 s67, s67, 2
	s_add_u32 s26, s26, 0x100
	s_addc_u32 s27, s27, 0
	s_cmp_gt_u32 s67, 5
	s_cbranch_scc0 .LBB0_249
	s_ashr_i32 s69, s68, 31
	s_lshl_b32 s66, s66, 7
	s_lshl_b64 s[26:27], s[68:69], 13
	v_or_b32_e32 v2, s66, v169
	s_add_u32 s26, s5, s26
	s_addc_u32 s27, s14, s27
	v_ashrrev_i32_e32 v3, 31, v2
	v_lshl_add_u64 v[6:7], v[2:3], 2, s[26:27]
	s_mov_b64 s[26:27], 0x1000
	v_lshl_add_u64 v[14:15], v[6:7], 0, s[26:27]
	ds_read_b128 v[2:5], v233 offset:64
	ds_read_b128 v[10:13], v233
	v_add_co_u32_e32 v6, vcc, s9, v6
	v_lshl_add_u32 v22, s75, 8, v171
	s_nop 0
	v_addc_co_u32_e32 v7, vcc, 0, v7, vcc
	ds_read_b128 v[6:9], v233 offset:128
	s_nop 0
	ds_read_b128 v[14:17], v233 offset:192
	s_and_b64 vcc, exec, s[58:59]
	s_cbranch_vccz .LBB0_252
	s_barrier
.LBB0_252:
	s_nop 15
	s_nop 15
	v_ashrrev_i32_e32 v23, 31, v22
	s_ashr_i32 s67, s66, 31
	s_mov_b64 s[26:27], -1
	s_and_b64 vcc, exec, s[38:39]
	s_waitcnt vmcnt(0)
	s_waitcnt lgkmcnt(0)
	v_pk_fma_f32 v[26:27], v[154:155], s[24:25], v[2:3] op_sel_hi:[1,0,1]
	v_pk_fma_f32 v[18:19], v[160:161], s[24:25], v[12:13] op_sel_hi:[1,0,1]
	v_pk_fma_f32 v[20:21], v[158:159], s[24:25], v[10:11] op_sel_hi:[1,0,1]
	v_min_f32_e32 v18, 0x40e00000, v18
	v_min_f32_e32 v20, 0x40e00000, v20
	v_min_f32_e32 v21, 0x40e00000, v21
	v_pk_fma_f32 v[30:31], v[150:151], s[24:25], v[6:7] op_sel_hi:[1,0,1]
	v_min_f32_e32 v19, 0x40e00000, v19
	v_med3_f32 v30, v30, s19, v227
	v_med3_f32 v31, v31, s19, v227
	v_pk_add_f32 v[30:31], v[30:31], 1.0 op_sel_hi:[1,0]
	v_pk_fma_f32 v[32:33], v[148:149], s[24:25], v[16:17] op_sel_hi:[1,0,1]
	v_pk_mul_f32 v[148:149], v[20:21], s[28:29] op_sel_hi:[1,0]
	v_pk_mul_f32 v[20:21], v[20:21], v[30:31]
	v_pk_mul_f32 v[30:31], v[18:19], s[28:29] op_sel_hi:[1,0]
	v_pk_fma_f32 v[24:25], v[152:153], s[24:25], v[8:9] op_sel_hi:[1,0,1]
	v_exp_f32_e32 v30, v30
	v_exp_f32_e32 v31, v31
	v_med3_f32 v24, v24, s19, v227
	v_med3_f32 v25, v25, s19, v227
	v_pk_add_f32 v[24:25], v[24:25], 1.0 op_sel_hi:[1,0]
	v_pk_add_f32 v[30:31], v[30:31], 1.0 op_sel_hi:[1,0]
	v_pk_mul_f32 v[18:19], v[18:19], v[24:25]
	v_rcp_f32_e32 v30, v30
	v_rcp_f32_e32 v31, v31
	v_pk_fma_f32 v[146:147], v[146:147], s[24:25], v[14:15] op_sel_hi:[1,0,1]
	v_pk_fma_f32 v[28:29], v[156:157], s[24:25], v[4:5] op_sel_hi:[1,0,1]
	v_exp_f32_e32 v148, v148
	v_pk_mul_f32 v[24:25], v[18:19], v[30:31]
	v_min_f32_e32 v18, 0x40e00000, v26
	v_min_f32_e32 v19, 0x40e00000, v27
	v_pk_mul_f32 v[30:31], v[18:19], s[28:29] op_sel_hi:[1,0]
	v_med3_f32 v26, v146, s19, v227
	v_exp_f32_e32 v30, v30
	v_exp_f32_e32 v31, v31
	v_med3_f32 v27, v147, s19, v227
	v_pk_add_f32 v[26:27], v[26:27], 1.0 op_sel_hi:[1,0]
	v_exp_f32_e32 v149, v149
	v_pk_add_f32 v[30:31], v[30:31], 1.0 op_sel_hi:[1,0]
	v_pk_mul_f32 v[18:19], v[18:19], v[26:27]
	v_rcp_f32_e32 v30, v30
	v_rcp_f32_e32 v31, v31
	v_pk_add_f32 v[148:149], v[148:149], 1.0 op_sel_hi:[1,0]
	v_pk_fma_f32 v[134:135], v[134:135], s[24:25], v[6:7] op_sel_hi:[1,0,1]
	v_rcp_f32_e32 v148, v148
	v_pk_mul_f32 v[26:27], v[18:19], v[30:31]
	v_min_f32_e32 v18, 0x40e00000, v28
	v_min_f32_e32 v19, 0x40e00000, v29
	v_pk_mul_f32 v[30:31], v[18:19], s[28:29] op_sel_hi:[1,0]
	v_rcp_f32_e32 v149, v149
	v_exp_f32_e32 v30, v30
	v_exp_f32_e32 v31, v31
	v_med3_f32 v28, v32, s19, v227
	v_med3_f32 v29, v33, s19, v227
	v_pk_add_f32 v[28:29], v[28:29], 1.0 op_sel_hi:[1,0]
	v_pk_add_f32 v[30:31], v[30:31], 1.0 op_sel_hi:[1,0]
	v_pk_mul_f32 v[18:19], v[18:19], v[28:29]
	v_rcp_f32_e32 v30, v30
	v_rcp_f32_e32 v31, v31
	v_pk_mul_f32 v[20:21], v[20:21], v[148:149]
	v_pk_fma_f32 v[32:33], v[136:137], s[24:25], v[8:9] op_sel_hi:[1,0,1]
	v_pk_fma_f32 v[142:143], v[142:143], s[24:25], v[10:11] op_sel_hi:[1,0,1]
	v_pk_mul_f32 v[28:29], v[18:19], v[30:31]
	v_mov_b32_e32 v19, v1
	v_mov_b32_e32 v18, v1
	v_cvt_pk_fp8_f32 v19, v26, v27
	v_cvt_pk_fp8_f32 v18, v20, v21
	v_pk_fma_f32 v[30:31], v[144:145], s[24:25], v[12:13] op_sel_hi:[1,0,1]
	v_pk_fma_f32 v[20:21], v[140:141], s[24:25], v[4:5] op_sel_hi:[1,0,1]
	v_cvt_pk_fp8_f32 v19, v28, v29 op_sel:[0,0,1]
	v_pk_fma_f32 v[28:29], v[130:131], s[24:25], v[14:15] op_sel_hi:[1,0,1]
	v_cvt_pk_fp8_f32 v18, v24, v25 op_sel:[0,0,1]
	v_pk_fma_f32 v[26:27], v[138:139], s[24:25], v[2:3] op_sel_hi:[1,0,1]
	v_pk_fma_f32 v[24:25], v[132:133], s[24:25], v[16:17] op_sel_hi:[1,0,1]
	v_med3_f32 v132, v134, s19, v227
	v_med3_f32 v133, v135, s19, v227
	v_med3_f32 v32, v32, s19, v227
	v_med3_f32 v33, v33, s19, v227
	v_med3_f32 v28, v28, s19, v227
	v_med3_f32 v29, v29, s19, v227
	v_min_f32_e32 v130, 0x40e00000, v142
	v_min_f32_e32 v131, 0x40e00000, v143
	v_pk_add_f32 v[132:133], v[132:133], 1.0 op_sel_hi:[1,0]
	v_min_f32_e32 v30, 0x40e00000, v30
	v_min_f32_e32 v31, 0x40e00000, v31
	v_pk_add_f32 v[32:33], v[32:33], 1.0 op_sel_hi:[1,0]
	v_min_f32_e32 v26, 0x40e00000, v26
	v_min_f32_e32 v27, 0x40e00000, v27
	v_pk_add_f32 v[28:29], v[28:29], 1.0 op_sel_hi:[1,0]
	v_min_f32_e32 v20, 0x40e00000, v20
	v_min_f32_e32 v21, 0x40e00000, v21
	v_pk_mul_f32 v[134:135], v[130:131], s[28:29] op_sel_hi:[1,0]
	v_pk_mul_f32 v[130:131], v[130:131], v[132:133]
	v_pk_mul_f32 v[132:133], v[30:31], s[28:29] op_sel_hi:[1,0]
	v_pk_mul_f32 v[30:31], v[30:31], v[32:33]
	v_pk_mul_f32 v[32:33], v[26:27], s[28:29] op_sel_hi:[1,0]
	v_pk_mul_f32 v[26:27], v[26:27], v[28:29]
	v_pk_mul_f32 v[28:29], v[20:21], s[28:29] op_sel_hi:[1,0]
	v_exp_f32_e32 v134, v134
	v_exp_f32_e32 v135, v135
	v_exp_f32_e32 v32, v32
	v_exp_f32_e32 v33, v33
	v_exp_f32_e32 v28, v28
	v_exp_f32_e32 v29, v29
	v_pk_add_f32 v[134:135], v[134:135], 1.0 op_sel_hi:[1,0]
	v_exp_f32_e32 v132, v132
	v_exp_f32_e32 v133, v133
	v_pk_add_f32 v[32:33], v[32:33], 1.0 op_sel_hi:[1,0]
	v_pk_add_f32 v[28:29], v[28:29], 1.0 op_sel_hi:[1,0]
	v_rcp_f32_e32 v134, v134
	v_rcp_f32_e32 v135, v135
	v_rcp_f32_e32 v32, v32
	v_rcp_f32_e32 v33, v33
	v_rcp_f32_e32 v28, v28
	v_rcp_f32_e32 v29, v29
	v_med3_f32 v24, v24, s19, v227
	v_med3_f32 v25, v25, s19, v227
	v_pk_add_f32 v[24:25], v[24:25], 1.0 op_sel_hi:[1,0]
	v_pk_add_f32 v[132:133], v[132:133], 1.0 op_sel_hi:[1,0]
	v_pk_mul_f32 v[20:21], v[20:21], v[24:25]
	v_pk_mul_f32 v[130:131], v[130:131], v[134:135]
	v_rcp_f32_e32 v132, v132
	v_rcp_f32_e32 v133, v133
	v_pk_mul_f32 v[26:27], v[26:27], v[32:33]
	v_pk_mul_f32 v[24:25], v[20:21], v[28:29]
	v_mov_b32_e32 v20, v1
	v_mov_b32_e32 v21, v1
	v_cvt_pk_fp8_f32 v20, v130, v131
	v_cvt_pk_fp8_f32 v21, v26, v27
	v_pk_mul_f32 v[30:31], v[30:31], v[132:133]
	v_pk_fma_f32 v[32:33], v[116:117], s[24:25], v[16:17] op_sel_hi:[1,0,1]
	v_cvt_pk_fp8_f32 v20, v30, v31 op_sel:[0,0,1]
	v_cvt_pk_fp8_f32 v21, v24, v25 op_sel:[0,0,1]
	v_lshlrev_b64 v[24:25], 10, v[22:23]
	v_lshl_add_u64 v[24:25], s[50:51], 0, v[24:25]
	v_lshl_add_u64 v[24:25], v[24:25], 0, s[66:67]
	v_lshl_add_u64 v[24:25], v[24:25], 0, s[52:53]
	v_permlane16_swap_b32_e32 v18, v20
	v_permlane16_swap_b32_e32 v19, v21
	v_lshl_add_u64 v[24:25], v[24:25], 0, v[166:167]
	v_pk_fma_f32 v[30:31], v[118:119], s[24:25], v[6:7] op_sel_hi:[1,0,1]
	global_store_dwordx4 v[24:25], v[18:21], off
	v_med3_f32 v30, v30, s19, v227
	v_med3_f32 v31, v31, s19, v227
	v_pk_fma_f32 v[18:19], v[128:129], s[24:25], v[12:13] op_sel_hi:[1,0,1]
	v_pk_fma_f32 v[20:21], v[126:127], s[24:25], v[10:11] op_sel_hi:[1,0,1]
	v_pk_add_f32 v[30:31], v[30:31], 1.0 op_sel_hi:[1,0]
	v_min_f32_e32 v20, 0x40e00000, v20
	v_min_f32_e32 v21, 0x40e00000, v21
	v_min_f32_e32 v18, 0x40e00000, v18
	v_min_f32_e32 v19, 0x40e00000, v19
	v_pk_mul_f32 v[116:117], v[20:21], s[28:29] op_sel_hi:[1,0]
	v_pk_mul_f32 v[20:21], v[20:21], v[30:31]
	v_pk_mul_f32 v[30:31], v[18:19], s[28:29] op_sel_hi:[1,0]
	v_pk_fma_f32 v[28:29], v[120:121], s[24:25], v[8:9] op_sel_hi:[1,0,1]
	v_exp_f32_e32 v30, v30
	v_exp_f32_e32 v31, v31
	v_med3_f32 v28, v28, s19, v227
	v_med3_f32 v29, v29, s19, v227
	v_pk_add_f32 v[28:29], v[28:29], 1.0 op_sel_hi:[1,0]
	v_pk_add_f32 v[30:31], v[30:31], 1.0 op_sel_hi:[1,0]
	v_pk_fma_f32 v[26:27], v[122:123], s[24:25], v[2:3] op_sel_hi:[1,0,1]
	v_rcp_f32_e32 v30, v30
	v_rcp_f32_e32 v31, v31
	v_pk_mul_f32 v[18:19], v[18:19], v[28:29]
	v_pk_fma_f32 v[114:115], v[114:115], s[24:25], v[14:15] op_sel_hi:[1,0,1]
	v_pk_fma_f32 v[24:25], v[124:125], s[24:25], v[4:5] op_sel_hi:[1,0,1]
	v_pk_mul_f32 v[28:29], v[18:19], v[30:31]
	v_min_f32_e32 v18, 0x40e00000, v26
	v_min_f32_e32 v19, 0x40e00000, v27
	v_pk_mul_f32 v[30:31], v[18:19], s[28:29] op_sel_hi:[1,0]
	v_med3_f32 v26, v114, s19, v227
	v_exp_f32_e32 v30, v30
	v_exp_f32_e32 v31, v31
	v_med3_f32 v27, v115, s19, v227
	v_pk_add_f32 v[26:27], v[26:27], 1.0 op_sel_hi:[1,0]
	v_exp_f32_e32 v116, v116
	v_pk_add_f32 v[30:31], v[30:31], 1.0 op_sel_hi:[1,0]
	v_pk_mul_f32 v[18:19], v[18:19], v[26:27]
	v_rcp_f32_e32 v30, v30
	v_rcp_f32_e32 v31, v31
	v_exp_f32_e32 v117, v117
	v_pk_fma_f32 v[98:99], v[98:99], s[24:25], v[14:15] op_sel_hi:[1,0,1]
	v_pk_fma_f32 v[100:101], v[100:101], s[24:25], v[16:17] op_sel_hi:[1,0,1]
	v_pk_mul_f32 v[26:27], v[18:19], v[30:31]
	v_min_f32_e32 v18, 0x40e00000, v24
	v_min_f32_e32 v19, 0x40e00000, v25
	v_pk_mul_f32 v[30:31], v[18:19], s[28:29] op_sel_hi:[1,0]
	v_med3_f32 v24, v32, s19, v227
	v_exp_f32_e32 v30, v30
	v_exp_f32_e32 v31, v31
	v_med3_f32 v25, v33, s19, v227
	v_pk_add_f32 v[24:25], v[24:25], 1.0 op_sel_hi:[1,0]
	v_pk_add_f32 v[116:117], v[116:117], 1.0 op_sel_hi:[1,0]
	v_pk_add_f32 v[30:31], v[30:31], 1.0 op_sel_hi:[1,0]
	v_pk_mul_f32 v[18:19], v[18:19], v[24:25]
	v_rcp_f32_e32 v30, v30
	v_rcp_f32_e32 v31, v31
	v_rcp_f32_e32 v116, v116
	v_rcp_f32_e32 v117, v117
	v_pk_fma_f32 v[32:33], v[102:103], s[24:25], v[6:7] op_sel_hi:[1,0,1]
	v_pk_mul_f32 v[24:25], v[18:19], v[30:31]
	v_mov_b32_e32 v19, v1
	v_cvt_pk_fp8_f32 v19, v26, v27
	v_pk_mul_f32 v[20:21], v[20:21], v[116:117]
	v_mov_b32_e32 v18, v1
	v_cvt_pk_fp8_f32 v18, v20, v21
	v_cvt_pk_fp8_f32 v19, v24, v25 op_sel:[0,0,1]
	v_pk_fma_f32 v[20:21], v[112:113], s[24:25], v[12:13] op_sel_hi:[1,0,1]
	v_pk_fma_f32 v[24:25], v[110:111], s[24:25], v[10:11] op_sel_hi:[1,0,1]
	v_med3_f32 v32, v32, s19, v227
	v_med3_f32 v33, v33, s19, v227
	v_min_f32_e32 v24, 0x40e00000, v24
	v_min_f32_e32 v25, 0x40e00000, v25
	v_pk_add_f32 v[32:33], v[32:33], 1.0 op_sel_hi:[1,0]
	v_min_f32_e32 v20, 0x40e00000, v20
	v_min_f32_e32 v21, 0x40e00000, v21
	v_pk_mul_f32 v[102:103], v[24:25], s[28:29] op_sel_hi:[1,0]
	v_pk_mul_f32 v[24:25], v[24:25], v[32:33]
	v_pk_mul_f32 v[32:33], v[20:21], s[28:29] op_sel_hi:[1,0]
	v_pk_fma_f32 v[30:31], v[104:105], s[24:25], v[8:9] op_sel_hi:[1,0,1]
	v_exp_f32_e32 v32, v32
	v_exp_f32_e32 v33, v33
	v_med3_f32 v30, v30, s19, v227
	v_med3_f32 v31, v31, s19, v227
	v_pk_add_f32 v[30:31], v[30:31], 1.0 op_sel_hi:[1,0]
	v_pk_add_f32 v[32:33], v[32:33], 1.0 op_sel_hi:[1,0]
	v_cvt_pk_fp8_f32 v18, v28, v29 op_sel:[0,0,1]
	v_rcp_f32_e32 v32, v32
	v_rcp_f32_e32 v33, v33
	v_pk_fma_f32 v[28:29], v[106:107], s[24:25], v[2:3] op_sel_hi:[1,0,1]
	v_pk_mul_f32 v[20:21], v[20:21], v[30:31]
	v_pk_fma_f32 v[26:27], v[108:109], s[24:25], v[4:5] op_sel_hi:[1,0,1]
	v_pk_mul_f32 v[30:31], v[20:21], v[32:33]
	v_min_f32_e32 v20, 0x40e00000, v28
	v_min_f32_e32 v21, 0x40e00000, v29
	v_pk_mul_f32 v[32:33], v[20:21], s[28:29] op_sel_hi:[1,0]
	v_med3_f32 v28, v98, s19, v227
	v_exp_f32_e32 v32, v32
	v_exp_f32_e32 v33, v33
	v_med3_f32 v29, v99, s19, v227
	v_pk_add_f32 v[28:29], v[28:29], 1.0 op_sel_hi:[1,0]
	v_exp_f32_e32 v102, v102
	v_pk_add_f32 v[32:33], v[32:33], 1.0 op_sel_hi:[1,0]
	v_pk_mul_f32 v[20:21], v[20:21], v[28:29]
	v_rcp_f32_e32 v32, v32
	v_rcp_f32_e32 v33, v33
	v_exp_f32_e32 v103, v103
	v_pk_fma_f32 v[82:83], v[82:83], s[24:25], v[14:15] op_sel_hi:[1,0,1]
	v_pk_fma_f32 v[84:85], v[84:85], s[24:25], v[16:17] op_sel_hi:[1,0,1]
	v_pk_mul_f32 v[28:29], v[20:21], v[32:33]
	v_min_f32_e32 v20, 0x40e00000, v26
	v_min_f32_e32 v21, 0x40e00000, v27
	v_pk_mul_f32 v[32:33], v[20:21], s[28:29] op_sel_hi:[1,0]
	v_pk_add_f32 v[102:103], v[102:103], 1.0 op_sel_hi:[1,0]
	v_exp_f32_e32 v32, v32
	v_exp_f32_e32 v33, v33
	v_rcp_f32_e32 v102, v102
	v_rcp_f32_e32 v103, v103
	v_med3_f32 v26, v100, s19, v227
	v_pk_add_f32 v[32:33], v[32:33], 1.0 op_sel_hi:[1,0]
	v_med3_f32 v27, v101, s19, v227
	v_rcp_f32_e32 v32, v32
	v_rcp_f32_e32 v33, v33
	v_pk_add_f32 v[26:27], v[26:27], 1.0 op_sel_hi:[1,0]
	v_pk_mul_f32 v[24:25], v[24:25], v[102:103]
	v_pk_mul_f32 v[20:21], v[20:21], v[26:27]
	s_nop 0
	v_pk_mul_f32 v[26:27], v[20:21], v[32:33]
	v_mov_b32_e32 v20, v1
	v_mov_b32_e32 v21, v1
	v_cvt_pk_fp8_f32 v20, v24, v25
	v_cvt_pk_fp8_f32 v21, v28, v29
	v_or_b32_e32 v24, 32, v22
	v_ashrrev_i32_e32 v25, 31, v24
	v_cvt_pk_fp8_f32 v20, v30, v31 op_sel:[0,0,1]
	v_cvt_pk_fp8_f32 v21, v26, v27 op_sel:[0,0,1]
	v_lshlrev_b64 v[24:25], 10, v[24:25]
	v_lshl_add_u64 v[24:25], s[50:51], 0, v[24:25]
	v_lshl_add_u64 v[24:25], v[24:25], 0, s[66:67]
	v_lshl_add_u64 v[24:25], v[24:25], 0, s[52:53]
	v_permlane16_swap_b32_e32 v18, v20
	v_permlane16_swap_b32_e32 v19, v21
	v_lshl_add_u64 v[24:25], v[24:25], 0, v[166:167]
	v_pk_fma_f32 v[32:33], v[86:87], s[24:25], v[6:7] op_sel_hi:[1,0,1]
	global_store_dwordx4 v[24:25], v[18:21], off
	v_med3_f32 v32, v32, s19, v227
	v_med3_f32 v33, v33, s19, v227
	v_pk_fma_f32 v[18:19], v[96:97], s[24:25], v[12:13] op_sel_hi:[1,0,1]
	v_pk_fma_f32 v[20:21], v[94:95], s[24:25], v[10:11] op_sel_hi:[1,0,1]
	v_pk_add_f32 v[32:33], v[32:33], 1.0 op_sel_hi:[1,0]
	v_min_f32_e32 v20, 0x40e00000, v20
	v_min_f32_e32 v21, 0x40e00000, v21
	v_min_f32_e32 v18, 0x40e00000, v18
	v_min_f32_e32 v19, 0x40e00000, v19
	v_pk_mul_f32 v[86:87], v[20:21], s[28:29] op_sel_hi:[1,0]
	v_pk_mul_f32 v[20:21], v[20:21], v[32:33]
	v_pk_mul_f32 v[32:33], v[18:19], s[28:29] op_sel_hi:[1,0]
	v_pk_fma_f32 v[30:31], v[88:89], s[24:25], v[8:9] op_sel_hi:[1,0,1]
	v_exp_f32_e32 v32, v32
	v_exp_f32_e32 v33, v33
	v_med3_f32 v30, v30, s19, v227
	v_med3_f32 v31, v31, s19, v227
	v_pk_add_f32 v[30:31], v[30:31], 1.0 op_sel_hi:[1,0]
	v_pk_add_f32 v[32:33], v[32:33], 1.0 op_sel_hi:[1,0]
	v_pk_fma_f32 v[28:29], v[90:91], s[24:25], v[2:3] op_sel_hi:[1,0,1]
	v_rcp_f32_e32 v32, v32
	v_rcp_f32_e32 v33, v33
	v_pk_mul_f32 v[18:19], v[18:19], v[30:31]
	v_pk_fma_f32 v[26:27], v[92:93], s[24:25], v[4:5] op_sel_hi:[1,0,1]
	v_exp_f32_e32 v86, v86
	v_pk_mul_f32 v[30:31], v[18:19], v[32:33]
	v_min_f32_e32 v18, 0x40e00000, v28
	v_min_f32_e32 v19, 0x40e00000, v29
	v_pk_mul_f32 v[32:33], v[18:19], s[28:29] op_sel_hi:[1,0]
	v_med3_f32 v28, v82, s19, v227
	v_exp_f32_e32 v32, v32
	v_exp_f32_e32 v33, v33
	v_med3_f32 v29, v83, s19, v227
	v_pk_add_f32 v[28:29], v[28:29], 1.0 op_sel_hi:[1,0]
	v_exp_f32_e32 v87, v87
	v_pk_add_f32 v[32:33], v[32:33], 1.0 op_sel_hi:[1,0]
	v_pk_mul_f32 v[18:19], v[18:19], v[28:29]
	v_rcp_f32_e32 v32, v32
	v_rcp_f32_e32 v33, v33
	v_pk_add_f32 v[86:87], v[86:87], 1.0 op_sel_hi:[1,0]
	v_add_u32_e32 v24, 0x80, v22
	v_rcp_f32_e32 v86, v86
	v_pk_mul_f32 v[28:29], v[18:19], v[32:33]
	v_min_f32_e32 v18, 0x40e00000, v26
	v_min_f32_e32 v19, 0x40e00000, v27
	v_pk_mul_f32 v[32:33], v[18:19], s[28:29] op_sel_hi:[1,0]
	v_rcp_f32_e32 v87, v87
	v_exp_f32_e32 v32, v32
	v_exp_f32_e32 v33, v33
	v_med3_f32 v26, v84, s19, v227
	v_med3_f32 v27, v85, s19, v227
	v_pk_add_f32 v[26:27], v[26:27], 1.0 op_sel_hi:[1,0]
	v_pk_add_f32 v[32:33], v[32:33], 1.0 op_sel_hi:[1,0]
	v_pk_mul_f32 v[18:19], v[18:19], v[26:27]
	v_rcp_f32_e32 v32, v32
	v_rcp_f32_e32 v33, v33
	v_pk_mul_f32 v[20:21], v[20:21], v[86:87]
	v_ashrrev_i32_e32 v25, 31, v24
	v_lshlrev_b64 v[24:25], 10, v[24:25]
	v_pk_mul_f32 v[26:27], v[18:19], v[32:33]
	v_mov_b32_e32 v18, v1
	v_cvt_pk_fp8_f32 v18, v20, v21
	v_mov_b32_e32 v19, v1
	v_cvt_pk_fp8_f32 v19, v28, v29
	v_pk_fma_f32 v[20:21], v[72:73], s[24:25], v[12:13] op_sel_hi:[1,0,1]
	v_cvt_pk_fp8_f32 v18, v30, v31 op_sel:[0,0,1]
	v_pk_fma_f32 v[30:31], v[66:67], s[24:25], v[2:3] op_sel_hi:[1,0,1]
	v_pk_fma_f32 v[66:67], v[78:79], s[24:25], v[6:7] op_sel_hi:[1,0,1]
	v_cvt_pk_fp8_f32 v19, v26, v27 op_sel:[0,0,1]
	v_pk_fma_f32 v[26:27], v[70:71], s[24:25], v[10:11] op_sel_hi:[1,0,1]
	v_med3_f32 v66, v66, s19, v227
	v_med3_f32 v67, v67, s19, v227
	v_min_f32_e32 v26, 0x40e00000, v26
	v_min_f32_e32 v27, 0x40e00000, v27
	v_pk_add_f32 v[66:67], v[66:67], 1.0 op_sel_hi:[1,0]
	v_min_f32_e32 v20, 0x40e00000, v20
	v_min_f32_e32 v21, 0x40e00000, v21
	v_pk_mul_f32 v[72:73], v[26:27], s[28:29] op_sel_hi:[1,0]
	v_pk_mul_f32 v[26:27], v[26:27], v[66:67]
	v_pk_mul_f32 v[66:67], v[20:21], s[28:29] op_sel_hi:[1,0]
	v_pk_fma_f32 v[32:33], v[80:81], s[24:25], v[8:9] op_sel_hi:[1,0,1]
	v_exp_f32_e32 v66, v66
	v_exp_f32_e32 v67, v67
	v_med3_f32 v32, v32, s19, v227
	v_med3_f32 v33, v33, s19, v227
	v_pk_add_f32 v[32:33], v[32:33], 1.0 op_sel_hi:[1,0]
	v_pk_add_f32 v[66:67], v[66:67], 1.0 op_sel_hi:[1,0]
	v_pk_mul_f32 v[20:21], v[20:21], v[32:33]
	v_rcp_f32_e32 v66, v66
	v_rcp_f32_e32 v67, v67
	v_pk_fma_f32 v[70:71], v[74:75], s[24:25], v[14:15] op_sel_hi:[1,0,1]
	v_pk_fma_f32 v[28:29], v[68:69], s[24:25], v[4:5] op_sel_hi:[1,0,1]
	v_exp_f32_e32 v72, v72
	v_pk_mul_f32 v[32:33], v[20:21], v[66:67]
	v_min_f32_e32 v20, 0x40e00000, v30
	v_min_f32_e32 v21, 0x40e00000, v31
	v_pk_mul_f32 v[66:67], v[20:21], s[28:29] op_sel_hi:[1,0]
	v_med3_f32 v30, v70, s19, v227
	v_exp_f32_e32 v66, v66
	v_exp_f32_e32 v67, v67
	v_med3_f32 v31, v71, s19, v227
	v_pk_add_f32 v[30:31], v[30:31], 1.0 op_sel_hi:[1,0]
	v_exp_f32_e32 v73, v73
	v_pk_add_f32 v[66:67], v[66:67], 1.0 op_sel_hi:[1,0]
	v_pk_mul_f32 v[20:21], v[20:21], v[30:31]
	v_rcp_f32_e32 v66, v66
	v_rcp_f32_e32 v67, v67
	v_pk_add_f32 v[72:73], v[72:73], 1.0 op_sel_hi:[1,0]
	v_pk_fma_f32 v[68:69], v[76:77], s[24:25], v[16:17] op_sel_hi:[1,0,1]
	v_rcp_f32_e32 v72, v72
	v_pk_mul_f32 v[30:31], v[20:21], v[66:67]
	v_min_f32_e32 v20, 0x40e00000, v28
	v_min_f32_e32 v21, 0x40e00000, v29
	v_pk_mul_f32 v[66:67], v[20:21], s[28:29] op_sel_hi:[1,0]
	v_rcp_f32_e32 v73, v73
	v_exp_f32_e32 v66, v66
	v_exp_f32_e32 v67, v67
	v_med3_f32 v28, v68, s19, v227
	v_med3_f32 v29, v69, s19, v227
	v_pk_add_f32 v[28:29], v[28:29], 1.0 op_sel_hi:[1,0]
	v_pk_add_f32 v[66:67], v[66:67], 1.0 op_sel_hi:[1,0]
	v_pk_mul_f32 v[20:21], v[20:21], v[28:29]
	v_rcp_f32_e32 v66, v66
	v_rcp_f32_e32 v67, v67
	v_pk_mul_f32 v[26:27], v[26:27], v[72:73]
	v_lshl_add_u64 v[24:25], s[50:51], 0, v[24:25]
	v_lshl_add_u64 v[24:25], v[24:25], 0, s[66:67]
	v_pk_mul_f32 v[28:29], v[20:21], v[66:67]
	v_mov_b32_e32 v20, v1
	v_mov_b32_e32 v21, v1
	v_cvt_pk_fp8_f32 v20, v26, v27
	v_cvt_pk_fp8_f32 v21, v30, v31
	v_lshl_add_u64 v[24:25], v[24:25], 0, s[52:53]
	v_lshl_add_u64 v[24:25], v[24:25], 0, v[166:167]
	v_cvt_pk_fp8_f32 v20, v32, v33 op_sel:[0,0,1]
	v_cvt_pk_fp8_f32 v21, v28, v29 op_sel:[0,0,1]
	v_pk_fma_f32 v[30:31], v[62:63], s[24:25], v[6:7] op_sel_hi:[1,0,1]
	v_pk_fma_f32 v[28:29], v[64:65], s[24:25], v[8:9] op_sel_hi:[1,0,1]
	v_permlane16_swap_b32_e32 v18, v20
	v_permlane16_swap_b32_e32 v19, v21
	global_store_dwordx4 v[24:25], v[18:21], off
	v_med3_f32 v30, v30, s19, v227
	v_med3_f32 v31, v31, s19, v227
	v_pk_fma_f32 v[18:19], v[56:57], s[24:25], v[12:13] op_sel_hi:[1,0,1]
	v_pk_fma_f32 v[20:21], v[54:55], s[24:25], v[10:11] op_sel_hi:[1,0,1]
	v_pk_add_f32 v[30:31], v[30:31], 1.0 op_sel_hi:[1,0]
	v_min_f32_e32 v20, 0x40e00000, v20
	v_min_f32_e32 v21, 0x40e00000, v21
	v_min_f32_e32 v18, 0x40e00000, v18
	v_min_f32_e32 v19, 0x40e00000, v19
	v_pk_fma_f32 v[24:25], v[52:53], s[24:25], v[4:5] op_sel_hi:[1,0,1]
	v_pk_mul_f32 v[52:53], v[20:21], s[28:29] op_sel_hi:[1,0]
	v_pk_mul_f32 v[20:21], v[20:21], v[30:31]
	v_pk_mul_f32 v[30:31], v[18:19], s[28:29] op_sel_hi:[1,0]
	v_med3_f32 v28, v28, s19, v227
	v_exp_f32_e32 v30, v30
	v_exp_f32_e32 v31, v31
	v_med3_f32 v29, v29, s19, v227
	v_pk_add_f32 v[28:29], v[28:29], 1.0 op_sel_hi:[1,0]
	v_pk_fma_f32 v[26:27], v[50:51], s[24:25], v[2:3] op_sel_hi:[1,0,1]
	v_pk_add_f32 v[30:31], v[30:31], 1.0 op_sel_hi:[1,0]
	v_pk_mul_f32 v[18:19], v[18:19], v[28:29]
	v_rcp_f32_e32 v30, v30
	v_rcp_f32_e32 v31, v31
	v_pk_fma_f32 v[50:51], v[58:59], s[24:25], v[14:15] op_sel_hi:[1,0,1]
	v_exp_f32_e32 v52, v52
	v_exp_f32_e32 v53, v53
	v_pk_mul_f32 v[28:29], v[18:19], v[30:31]
	v_min_f32_e32 v18, 0x40e00000, v26
	v_min_f32_e32 v19, 0x40e00000, v27
	v_pk_mul_f32 v[30:31], v[18:19], s[28:29] op_sel_hi:[1,0]
	v_med3_f32 v26, v50, s19, v227
	v_exp_f32_e32 v30, v30
	v_exp_f32_e32 v31, v31
	v_med3_f32 v27, v51, s19, v227
	v_pk_add_f32 v[26:27], v[26:27], 1.0 op_sel_hi:[1,0]
	v_pk_add_f32 v[52:53], v[52:53], 1.0 op_sel_hi:[1,0]
	v_pk_add_f32 v[30:31], v[30:31], 1.0 op_sel_hi:[1,0]
	v_pk_mul_f32 v[18:19], v[18:19], v[26:27]
	v_rcp_f32_e32 v30, v30
	v_rcp_f32_e32 v31, v31
	v_pk_fma_f32 v[32:33], v[60:61], s[24:25], v[16:17] op_sel_hi:[1,0,1]
	v_rcp_f32_e32 v52, v52
	v_rcp_f32_e32 v53, v53
	v_pk_mul_f32 v[26:27], v[18:19], v[30:31]
	v_min_f32_e32 v18, 0x40e00000, v24
	v_min_f32_e32 v19, 0x40e00000, v25
	v_pk_mul_f32 v[30:31], v[18:19], s[28:29] op_sel_hi:[1,0]
	v_med3_f32 v24, v32, s19, v227
	v_exp_f32_e32 v30, v30
	v_exp_f32_e32 v31, v31
	v_med3_f32 v25, v33, s19, v227
	v_pk_add_f32 v[24:25], v[24:25], 1.0 op_sel_hi:[1,0]
	v_pk_fma_f32 v[6:7], v[46:47], s[24:25], v[6:7] op_sel_hi:[1,0,1]
	v_pk_add_f32 v[30:31], v[30:31], 1.0 op_sel_hi:[1,0]
	v_pk_mul_f32 v[18:19], v[18:19], v[24:25]
	v_rcp_f32_e32 v30, v30
	v_rcp_f32_e32 v31, v31
	v_pk_fma_f32 v[10:11], v[38:39], s[24:25], v[10:11] op_sel_hi:[1,0,1]
	v_med3_f32 v6, v6, s19, v227
	v_med3_f32 v7, v7, s19, v227
	v_pk_mul_f32 v[20:21], v[20:21], v[52:53]
	v_pk_mul_f32 v[24:25], v[18:19], v[30:31]
	v_mov_b32_e32 v18, v1
	v_pk_fma_f32 v[12:13], v[40:41], s[24:25], v[12:13] op_sel_hi:[1,0,1]
	v_min_f32_e32 v10, 0x40e00000, v10
	v_min_f32_e32 v11, 0x40e00000, v11
	v_pk_add_f32 v[6:7], v[6:7], 1.0 op_sel_hi:[1,0]
	v_cvt_pk_fp8_f32 v18, v20, v21
	v_pk_mul_f32 v[20:21], v[10:11], s[28:29] op_sel_hi:[1,0]
	v_pk_mul_f32 v[6:7], v[10:11], v[6:7]
	v_min_f32_e32 v10, 0x40e00000, v12
	v_min_f32_e32 v11, 0x40e00000, v13
	v_pk_mul_f32 v[12:13], v[10:11], s[28:29] op_sel_hi:[1,0]
	v_pk_fma_f32 v[8:9], v[48:49], s[24:25], v[8:9] op_sel_hi:[1,0,1]
	v_exp_f32_e32 v12, v12
	v_exp_f32_e32 v13, v13
	v_med3_f32 v8, v8, s19, v227
	v_med3_f32 v9, v9, s19, v227
	v_pk_fma_f32 v[2:3], v[34:35], s[24:25], v[2:3] op_sel_hi:[1,0,1]
	v_pk_add_f32 v[12:13], v[12:13], 1.0 op_sel_hi:[1,0]
	v_pk_add_f32 v[8:9], v[8:9], 1.0 op_sel_hi:[1,0]
	v_rcp_f32_e32 v12, v12
	v_rcp_f32_e32 v13, v13
	v_pk_mul_f32 v[8:9], v[10:11], v[8:9]
	v_min_f32_e32 v2, 0x40e00000, v2
	v_min_f32_e32 v3, 0x40e00000, v3
	v_pk_mul_f32 v[8:9], v[8:9], v[12:13]
	v_pk_mul_f32 v[12:13], v[2:3], s[28:29] op_sel_hi:[1,0]
	v_pk_fma_f32 v[14:15], v[42:43], s[24:25], v[14:15] op_sel_hi:[1,0,1]
	v_exp_f32_e32 v12, v12
	v_exp_f32_e32 v13, v13
	v_exp_f32_e32 v20, v20
	v_exp_f32_e32 v21, v21
	v_med3_f32 v10, v14, s19, v227
	v_pk_add_f32 v[12:13], v[12:13], 1.0 op_sel_hi:[1,0]
	v_med3_f32 v11, v15, s19, v227
	v_rcp_f32_e32 v12, v12
	v_rcp_f32_e32 v13, v13
	v_pk_fma_f32 v[4:5], v[36:37], s[24:25], v[4:5] op_sel_hi:[1,0,1]
	v_pk_add_f32 v[10:11], v[10:11], 1.0 op_sel_hi:[1,0]
	v_min_f32_e32 v4, 0x40e00000, v4
	v_pk_mul_f32 v[2:3], v[2:3], v[10:11]
	v_min_f32_e32 v5, 0x40e00000, v5
	v_pk_mul_f32 v[2:3], v[2:3], v[12:13]
	v_pk_mul_f32 v[12:13], v[4:5], s[28:29] op_sel_hi:[1,0]
	v_pk_add_f32 v[20:21], v[20:21], 1.0 op_sel_hi:[1,0]
	v_exp_f32_e32 v12, v12
	v_exp_f32_e32 v13, v13
	v_rcp_f32_e32 v20, v20
	v_rcp_f32_e32 v21, v21
	v_mov_b32_e32 v19, v1
	v_pk_add_f32 v[12:13], v[12:13], 1.0 op_sel_hi:[1,0]
	v_pk_fma_f32 v[16:17], v[44:45], s[24:25], v[16:17] op_sel_hi:[1,0,1]
	v_pk_mul_f32 v[6:7], v[6:7], v[20:21]
	v_rcp_f32_e32 v12, v12
	v_rcp_f32_e32 v13, v13
	v_mov_b32_e32 v20, v1
	v_mov_b32_e32 v21, v1
	v_cvt_pk_fp8_f32 v19, v26, v27
	v_med3_f32 v10, v16, s19, v227
	v_med3_f32 v11, v17, s19, v227
	v_cvt_pk_fp8_f32 v20, v6, v7
	v_cvt_pk_fp8_f32 v21, v2, v3
	v_pk_add_f32 v[10:11], v[10:11], 1.0 op_sel_hi:[1,0]
	v_add_u32_e32 v2, 0xa0, v22
	v_pk_mul_f32 v[4:5], v[4:5], v[10:11]
	v_ashrrev_i32_e32 v3, 31, v2
	v_pk_mul_f32 v[4:5], v[4:5], v[12:13]
	v_cvt_pk_fp8_f32 v18, v28, v29 op_sel:[0,0,1]
	v_cvt_pk_fp8_f32 v19, v24, v25 op_sel:[0,0,1]
	v_cvt_pk_fp8_f32 v20, v8, v9 op_sel:[0,0,1]
	v_cvt_pk_fp8_f32 v21, v4, v5 op_sel:[0,0,1]
	v_lshlrev_b64 v[2:3], 10, v[2:3]
	v_lshl_add_u64 v[2:3], s[50:51], 0, v[2:3]
	v_lshl_add_u64 v[2:3], v[2:3], 0, s[66:67]
	v_lshl_add_u64 v[2:3], v[2:3], 0, s[52:53]
	v_permlane16_swap_b32_e32 v18, v20
	v_permlane16_swap_b32_e32 v19, v21
	v_lshl_add_u64 v[2:3], v[2:3], 0, v[166:167]
	global_store_dwordx4 v[2:3], v[18:21], off
	s_cbranch_vccnz .LBB0_237
	s_andn2_b64 vcc, exec, s[42:43]
	s_cbranch_vccnz .LBB0_236
	s_barrier
	s_branch .LBB0_236
